# attn_a main loop: QK MFMAs interleaved with softmax VALU in 2nd half-iteration, dead zero-init movs removed, dedicated all-ones MFMA operand regs, max-tree canonicalize ops removed (bit-identical)
# speedup vs baseline: 1.0074x; 1.0074x over previous
.LBB0_1285:
	s_lshl_b32 s6, s3, 7
	s_lshl_b64 s[0:1], s[0:1], 10
	s_ashr_i32 s39, s6, 31
	s_add_u32 s38, s0, s6
	s_addc_u32 s39, s1, s39
	s_mul_i32 s0, s27, 0x1100
	s_mul_hi_u32 s1, s26, 0x1100
	s_add_i32 s1, s1, s0
	s_mul_i32 s0, s26, 0x1100
	s_add_u32 s0, s36, s0
	s_addc_u32 s1, s37, s1
	s_lshl_b32 s3, s3, 5
	s_and_b32 s3, s3, 0xffffff80
	s_lshl_b64 s[0:1], s[0:1], 8
	s_ashr_i32 s6, s3, 31
	v_mov_b32_e32 v13, v0
	s_add_u32 s0, s0, s3
	s_movk_i32 s3, 0xffe0
	v_ashrrev_i32_e32 v8, 1, v13
	s_addc_u32 s1, s1, s6
	s_lshl_b64 s[26:27], s[38:39], 1
	v_bfi_b32 v4, s3, v8, v13
	s_add_u32 s36, s12, s26
	v_ashrrev_i32_e32 v5, 31, v4
	s_addc_u32 s37, s21, s27
	v_lshlrev_b64 v[4:5], 11, v[4:5]
	v_and_b32_e32 v12, 32, v13
	v_lshl_add_u64 v[4:5], s[36:37], 0, v[4:5]
	v_lshlrev_b32_e32 v2, 1, v12
	v_lshl_add_u64 v[30:31], v[4:5], 0, v[2:3]
	global_load_dwordx4 v[4:7], v[30:31], off
	global_load_dwordx4 v[14:17], v[30:31], off offset:16
	global_load_dwordx4 v[18:21], v[30:31], off offset:32
	global_load_dwordx4 v[22:25], v[30:31], off offset:48
	v_and_b32_e32 v164, 0xffffffe0, v8
	global_load_dwordx4 v[8:11], v[30:31], off offset:144
	global_load_dwordx4 v[26:29], v[30:31], off offset:128
	s_add_u32 s38, s25, s0
	s_addc_u32 s39, s35, s1
	s_add_u32 s36, s44, s0
	v_and_b32_e32 v2, 0x3fffffc0, v13
	s_addc_u32 s37, s45, s1
	s_add_i32 s3, 0, 0x10400
	v_lshl_add_u32 v165, v2, 2, s3
	v_mov_b32_e32 v124, v3
	v_mov_b32_e32 v125, v3
	v_mov_b32_e32 v126, v3
	v_mov_b32_e32 v127, v3
	v_mov_b32_e32 v129, v3
	v_mov_b32_e32 v128, v3
	v_mov_b32_e32 v130, v3
	v_mov_b32_e32 v131, v3
	v_mov_b32_e32 v132, v3
	v_mov_b32_e32 v133, v3
	v_mov_b32_e32 v134, v3
	v_mov_b32_e32 v135, v3
	v_mov_b32_e32 v136, v3
	v_mov_b32_e32 v137, v3
	v_mov_b32_e32 v138, v3
	v_mov_b32_e32 v139, v3
	v_and_b32_e32 v194, 31, v13
	v_lshlrev_b32_e32 v52, 7, v194
	s_add_i32 s3, 0, 0x400
	s_add_u32 s40, s36, 0x4000
	s_addc_u32 s41, s37, 0
	v_and_b32_e32 v68, 63, v13
	v_bfe_u32 v195, v13, 5, 1
	s_mov_b32 s76, s77
	s_mov_b32 s78, s77
	s_mov_b32 s79, s77
	s_mov_b32 s80, s77
	s_mov_b32 s81, s77
	s_mov_b32 s82, s77
	s_mov_b32 s83, s77
	s_mov_b32 s84, s77
	s_mov_b32 s85, s77
	s_mov_b32 s86, s77
	s_mov_b32 s87, s77
	s_mov_b32 s88, s77
	s_mov_b32 s89, s77
	s_mov_b32 s90, s77
	s_mov_b32 s91, s77
	s_mov_b32 s49, 2
	v_mov_b32_e32 v167, v3
	v_mov_b32_e32 v169, v3
	v_lshl_add_u32 v199, v194, 2, v165
	v_lshlrev_b32_e32 v198, 4, v195
	s_waitcnt vmcnt(5)
	v_lshlrev_b32_e32 v2, 16, v4
	v_and_b32_e32 v4, 0xffff0000, v4
	v_lshlrev_b32_e32 v33, 16, v6
	v_and_b32_e32 v6, 0xffff0000, v6
	s_waitcnt vmcnt(4)
	v_lshlrev_b32_e32 v35, 16, v14
	v_and_b32_e32 v14, 0xffff0000, v14
	v_lshlrev_b32_e32 v37, 16, v16
	v_and_b32_e32 v16, 0xffff0000, v16
	v_med3_f32 v2, v2, s7, v228
	v_med3_f32 v4, v4, s7, v228
	v_med3_f32 v33, v33, s7, v228
	v_med3_f32 v6, v6, s7, v228
	v_med3_f32 v35, v35, s7, v228
	v_med3_f32 v14, v14, s7, v228
	v_med3_f32 v37, v37, s7, v228
	v_med3_f32 v16, v16, s7, v228
	v_cvt_pk_fp8_f32 v124, v2, v4
	v_cvt_pk_fp8_f32 v125, v33, v6
	v_cvt_pk_fp8_f32 v126, v35, v14
	v_cvt_pk_fp8_f32 v127, v37, v16
	v_lshlrev_b32_e32 v32, 16, v5
	v_and_b32_e32 v5, 0xffff0000, v5
	v_lshlrev_b32_e32 v34, 16, v7
	v_and_b32_e32 v7, 0xffff0000, v7
	v_lshlrev_b32_e32 v36, 16, v15
	v_and_b32_e32 v15, 0xffff0000, v15
	v_lshlrev_b32_e32 v38, 16, v17
	v_and_b32_e32 v17, 0xffff0000, v17
	s_waitcnt vmcnt(3)
	v_lshlrev_b32_e32 v2, 16, v20
	v_and_b32_e32 v4, 0xffff0000, v20
	v_med3_f32 v32, v32, s7, v228
	v_med3_f32 v5, v5, s7, v228
	v_med3_f32 v34, v34, s7, v228
	v_med3_f32 v7, v7, s7, v228
	v_med3_f32 v36, v36, s7, v228
	v_med3_f32 v15, v15, s7, v228
	v_med3_f32 v38, v38, s7, v228
	v_med3_f32 v17, v17, s7, v228
	v_med3_f32 v2, v2, s7, v228
	v_med3_f32 v4, v4, s7, v228
	v_lshlrev_b32_e32 v39, 16, v18
	v_and_b32_e32 v18, 0xffff0000, v18
	v_cvt_pk_fp8_f32 v124, v32, v5 op_sel:[0,0,1]
	v_cvt_pk_fp8_f32 v125, v34, v7 op_sel:[0,0,1]
	v_cvt_pk_fp8_f32 v126, v36, v15 op_sel:[0,0,1]
	v_cvt_pk_fp8_f32 v127, v38, v17 op_sel:[0,0,1]
	v_cvt_pk_fp8_f32 v129, v2, v4
	global_load_dwordx4 v[4:7], v[30:31], off offset:176
	global_load_dwordx4 v[14:17], v[30:31], off offset:160
	v_med3_f32 v39, v39, s7, v228
	v_med3_f32 v18, v18, s7, v228
	v_cvt_pk_fp8_f32 v128, v39, v18
	v_lshlrev_b32_e32 v40, 16, v19
	v_and_b32_e32 v19, 0xffff0000, v19
	v_med3_f32 v40, v40, s7, v228
	v_med3_f32 v19, v19, s7, v228
	v_cvt_pk_fp8_f32 v128, v40, v19 op_sel:[0,0,1]
	v_lshlrev_b32_e32 v18, 16, v21
	v_and_b32_e32 v19, 0xffff0000, v21
	v_med3_f32 v2, v18, s7, v228
	v_med3_f32 v18, v19, s7, v228
	v_cvt_pk_fp8_f32 v129, v2, v18 op_sel:[0,0,1]
	s_waitcnt vmcnt(4)
	v_lshlrev_b32_e32 v2, 16, v22
	v_and_b32_e32 v18, 0xffff0000, v22
	v_med3_f32 v2, v2, s7, v228
	v_med3_f32 v18, v18, s7, v228
	v_cvt_pk_fp8_f32 v130, v2, v18
	v_lshlrev_b32_e32 v19, 16, v23
	v_and_b32_e32 v2, 0xffff0000, v23
	v_med3_f32 v18, v19, s7, v228
	v_med3_f32 v2, v2, s7, v228
	v_cvt_pk_fp8_f32 v130, v18, v2 op_sel:[0,0,1]
	v_lshlrev_b32_e32 v2, 16, v24
	v_and_b32_e32 v18, 0xffff0000, v24
	v_med3_f32 v2, v2, s7, v228
	v_med3_f32 v18, v18, s7, v228
	v_cvt_pk_fp8_f32 v131, v2, v18
	v_lshlrev_b32_e32 v19, 16, v25
	v_and_b32_e32 v2, 0xffff0000, v25
	v_med3_f32 v18, v19, s7, v228
	v_med3_f32 v2, v2, s7, v228
	v_cvt_pk_fp8_f32 v131, v18, v2 op_sel:[0,0,1]
	s_waitcnt vmcnt(2)
	v_lshlrev_b32_e32 v2, 16, v26
	v_and_b32_e32 v18, 0xffff0000, v26
	v_med3_f32 v2, v2, s7, v228
	v_med3_f32 v18, v18, s7, v228
	v_cvt_pk_fp8_f32 v132, v2, v18
	v_lshlrev_b32_e32 v19, 16, v27
	v_and_b32_e32 v2, 0xffff0000, v27
	v_med3_f32 v18, v19, s7, v228
	v_med3_f32 v2, v2, s7, v228
	v_cvt_pk_fp8_f32 v132, v18, v2 op_sel:[0,0,1]
	v_lshlrev_b32_e32 v2, 16, v28
	v_and_b32_e32 v18, 0xffff0000, v28
	v_med3_f32 v2, v2, s7, v228
	v_med3_f32 v18, v18, s7, v228
	v_cvt_pk_fp8_f32 v133, v2, v18
	v_lshlrev_b32_e32 v19, 16, v29
	v_and_b32_e32 v2, 0xffff0000, v29
	v_lshlrev_b32_e32 v27, 3, v13
	v_med3_f32 v18, v19, s7, v228
	v_med3_f32 v2, v2, s7, v228
	v_ashrrev_i32_e32 v26, 4, v13
	v_and_b32_e32 v28, 0x78, v27
	v_cvt_pk_fp8_f32 v133, v18, v2 op_sel:[0,0,1]
	v_lshlrev_b32_e32 v22, 16, v8
	v_lshl_or_b32 v2, v26, 9, v28
	v_and_b32_e32 v8, 0xffff0000, v8
	global_load_dwordx2 v[18:19], v2, s[36:37]
	global_load_dwordx2 v[20:21], v2, s[36:37] offset:256
	v_med3_f32 v22, v22, s7, v228
	v_med3_f32 v8, v8, s7, v228
	v_lshl_or_b32 v166, v26, 8, v28
	v_cvt_pk_fp8_f32 v134, v22, v8
	v_add_u32_e32 v168, 0x2000, v166
	global_load_dwordx2 v[22:23], v166, s[38:39]
	global_load_dwordx2 v[24:25], v168, s[38:39]
	v_lshlrev_b32_e32 v29, 16, v9
	v_and_b32_e32 v9, 0xffff0000, v9
	v_med3_f32 v8, v29, s7, v228
	v_med3_f32 v9, v9, s7, v228
	v_cvt_pk_fp8_f32 v134, v8, v9 op_sel:[0,0,1]
	v_lshlrev_b32_e32 v8, 16, v10
	v_and_b32_e32 v9, 0xffff0000, v10
	v_med3_f32 v8, v8, s7, v228
	v_med3_f32 v9, v9, s7, v228
	v_cvt_pk_fp8_f32 v135, v8, v9
	v_lshlrev_b32_e32 v10, 16, v11
	v_and_b32_e32 v8, 0xffff0000, v11
	v_med3_f32 v9, v10, s7, v228
	v_med3_f32 v8, v8, s7, v228
	v_cvt_pk_fp8_f32 v135, v9, v8 op_sel:[0,0,1]
	s_waitcnt vmcnt(4)
	v_lshlrev_b32_e32 v8, 16, v14
	v_and_b32_e32 v9, 0xffff0000, v14
	v_med3_f32 v8, v8, s7, v228
	v_med3_f32 v9, v9, s7, v228
	v_cvt_pk_fp8_f32 v136, v8, v9
	v_lshlrev_b32_e32 v10, 16, v15
	v_and_b32_e32 v8, 0xffff0000, v15
	v_med3_f32 v9, v10, s7, v228
	v_med3_f32 v8, v8, s7, v228
	v_cvt_pk_fp8_f32 v136, v9, v8 op_sel:[0,0,1]
	v_lshlrev_b32_e32 v8, 16, v16
	v_and_b32_e32 v9, 0xffff0000, v16
	v_med3_f32 v8, v8, s7, v228
	v_med3_f32 v9, v9, s7, v228
	v_cvt_pk_fp8_f32 v137, v8, v9
	v_lshlrev_b32_e32 v10, 16, v17
	v_and_b32_e32 v8, 0xffff0000, v17
	v_med3_f32 v9, v10, s7, v228
	v_med3_f32 v8, v8, s7, v228
	v_cvt_pk_fp8_f32 v137, v9, v8 op_sel:[0,0,1]
	v_lshlrev_b32_e32 v8, 16, v4
	v_and_b32_e32 v4, 0xffff0000, v4
	v_med3_f32 v8, v8, s7, v228
	v_med3_f32 v4, v4, s7, v228
	v_cvt_pk_fp8_f32 v138, v8, v4
	v_lshlrev_b32_e32 v9, 16, v5
	v_and_b32_e32 v4, 0xffff0000, v5
	v_med3_f32 v5, v9, s7, v228
	v_med3_f32 v4, v4, s7, v228
	v_cvt_pk_fp8_f32 v138, v5, v4 op_sel:[0,0,1]
	v_lshlrev_b32_e32 v4, 16, v6
	v_and_b32_e32 v5, 0xffff0000, v6
	v_med3_f32 v4, v4, s7, v228
	v_med3_f32 v5, v5, s7, v228
	v_cvt_pk_fp8_f32 v139, v4, v5
	v_and_b32_e32 v4, 0xfffff0, v26
	v_lshlrev_b32_e32 v5, 1, v26
	v_and_or_b32 v4, v5, 8, v4
	v_lshrrev_b32_e32 v4, 1, v4
	v_bfe_u32 v8, v27, 5, 2
	v_lshrrev_b32_e32 v5, 1, v26
	v_or_b32_e32 v4, v4, v8
	v_and_b32_e32 v8, 3, v26
	v_lshlrev_b32_e32 v36, 4, v13
	v_and_or_b32 v5, v5, 4, v8
	v_and_b32_e32 v8, 48, v36
	v_lshl_or_b32 v5, v5, 6, v8
	v_lshl_or_b32 v4, v4, 9, v5
	v_lshrrev_b32_e32 v5, 1, v13
	v_add_u32_e32 v200, 0, v4
	v_lshlrev_b32_e32 v4, 7, v26
	v_and_b32_e32 v5, 0x70, v5
	v_bitop3_b32 v4, v28, v4, v5 bitop3:0xde
	v_and_b32_e32 v53, 0x70, v27
	v_add_u32_e32 v202, 0, v4
	v_bitop3_b32 v4, v53, v52, v12 bitop3:0xde
	v_add_u32_e32 v201, 0, v4
	v_or_b32_e32 v4, 16, v12
	v_bitop3_b32 v4, v53, v52, v4 bitop3:0xde
	v_lshlrev_b32_e32 v6, 16, v7
	v_add_u32_e32 v203, 0, v4
	v_and_b32_e32 v4, 0xffff0000, v7
	s_waitcnt vmcnt(2)
	v_perm_b32 v8, v20, v18, s14
	v_perm_b32 v9, v20, v18, s15
	v_perm_b32 v10, v21, v19, s14
	v_perm_b32 v11, v21, v19, s15
	v_med3_f32 v5, v6, s7, v228
	v_med3_f32 v4, v4, s7, v228
	s_waitcnt vmcnt(0)
	ds_write_b128 v200, v[8:11] offset:1024
	s_waitcnt vmcnt(0)
	ds_write2st64_b64 v202, v[22:23], v[24:25] offset0:66 offset1:74
	s_waitcnt lgkmcnt(0)
	s_barrier
	ds_read_b128 v[14:17], v201 offset:33792
	ds_read_b128 v[18:21], v203 offset:33792
	v_cvt_pk_fp8_f32 v139, v5, v4 op_sel:[0,0,1]
	ds_read_b128 v[4:7], v201 offset:37888
	ds_read_b128 v[8:11], v203 offset:37888
	v_or_b32_e32 v69, 0x100, v2
	global_load_dwordx2 v[60:61], v2, s[40:41]
	global_load_dwordx2 v[62:63], v69, s[40:41]
	s_add_u32 s40, s38, 0x4000
	s_addc_u32 s41, s39, 0
	global_load_dwordx2 v[64:65], v166, s[40:41]
	global_load_dwordx2 v[66:67], v168, s[40:41]
	s_add_u32 s38, s38, 0x8000
	s_waitcnt lgkmcnt(2)
	v_mfma_scale_f32_32x32x64_f8f6f4 v[20:35], v[14:21], v[124:131], 0, v226, v226 op_sel_hi:[0,0,0]
	v_and_b32_e32 v15, 0xc0, v36
	s_addc_u32 s39, s39, 0
	s_add_u32 s36, s36, 0x8000
	s_addc_u32 s37, s37, 0
	v_lshlrev_b32_e32 v14, 3, v68
	v_lshlrev_b32_e32 v13, 1, v13
	v_and_or_b32 v15, v14, 24, v15
	v_and_b32_e32 v13, 32, v13
	s_waitcnt lgkmcnt(0)
	v_mfma_scale_f32_32x32x64_f8f6f4 v[36:51], v[4:11], v[124:131], 0, v226, v226 op_sel_hi:[0,0,0]
	v_or_b32_e32 v4, 64, v12
	v_or_b32_e32 v8, 0x50, v12
	v_bitop3_b32 v4, v53, v52, v4 bitop3:0xde
	v_bitop3_b32 v8, v53, v52, v8 bitop3:0xde
	v_add_u32_e32 v204, 0, v4
	v_add_u32_e32 v205, 0, v8
	ds_read_b128 v[4:7], v204 offset:33792
	ds_read_b128 v[8:11], v205 offset:33792
	ds_read_b128 v[52:55], v204 offset:37888
	ds_read_b128 v[56:59], v205 offset:37888
	global_load_dwordx2 v[170:171], v166, s[38:39]
	global_load_dwordx2 v[172:173], v168, s[38:39]
	global_load_dwordx2 v[176:177], v69, s[36:37]
	global_load_dwordx2 v[174:175], v2, s[36:37]
	s_waitcnt vmcnt(4)
	v_and_b32_e32 v12, 0x100, v14
	v_or3_b32 v70, v15, v13, v12
	v_add_u32_e32 v197, s3, v70
	s_waitcnt lgkmcnt(2)
	v_mfma_scale_f32_32x32x64_f8f6f4 v[20:35], v[4:11], v[132:139], v[20:35], v226, v226 op_sel_hi:[0,0,0]
	v_mov_b64_e32 v[4:5], s[76:77]
	v_mov_b64_e32 v[18:19], s[90:91]
	v_mov_b64_e32 v[6:7], s[78:79]
	v_mov_b64_e32 v[8:9], s[80:81]
	v_mov_b64_e32 v[10:11], s[82:83]
	v_mov_b64_e32 v[12:13], s[84:85]
	v_mov_b64_e32 v[14:15], s[86:87]
	v_mov_b64_e32 v[16:17], s[88:89]
	v_cmp_gt_u32_e64 s[38:39], 32, v68
	v_readlane_b32 s90, v254, 55
	v_readlane_b32 s86, v254, 57
	v_readlane_b32 s82, v254, 59
	v_readlane_b32 s84, v254, 61
	v_readlane_b32 s91, v254, 56
	v_readlane_b32 s87, v254, 58
	s_waitcnt lgkmcnt(0)
	v_mfma_scale_f32_32x32x64_f8f6f4 v[36:51], v[52:59], v[132:139], v[36:51], v226, v226 op_sel_hi:[0,0,0]
	s_nop 2
	v_max_f32_e32 v52, v21, v21
	v_max_f32_e32 v53, v20, v20
	v_max_f32_e32 v52, v53, v52
	v_max3_f32 v52, v52, v22, v23
	v_max3_f32 v52, v52, v24, v25
	v_max3_f32 v52, v52, v26, v27
	v_max3_f32 v52, v52, v28, v29
	v_max3_f32 v52, v52, v30, v31
	v_max3_f32 v52, v52, v32, v33
	v_max3_f32 v52, v52, v34, v35
	v_readlane_b32 s83, v254, 60
	v_readlane_b32 s85, v254, 62
	s_mov_b32 s88, 0x87ff
	s_movk_i32 s89, 0x1000
	s_nop 2
	v_max3_f32 v52, v52, v36, v37
	v_max3_f32 v52, v52, v38, v39
	v_max3_f32 v52, v52, v40, v41
	v_max3_f32 v52, v52, v42, v43
	v_max3_f32 v52, v52, v44, v45
	v_max3_f32 v52, v52, v46, v47
	v_max3_f32 v52, v52, v48, v49
	v_max3_f32 v52, v52, v50, v51
	v_mov_b32_e32 v53, v52
	s_nop 1
	v_permlane32_swap_b32_e32 v52, v53
	v_max_f32_e32 v53, v53, v53
	v_max_f32_e32 v52, v52, v52
	v_max_f32_e32 v56, v52, v53
	v_add_f32_e32 v52, 0x7149f2ca, v56
	v_cmp_ge_f32_e32 vcc, s19, v52
	s_waitcnt vmcnt(6)
	v_perm_b32 v52, v62, v60, s14
	v_perm_b32 v53, v62, v60, s15
	v_perm_b32 v54, v63, v61, s14
	v_perm_b32 v55, v63, v61, s15
	s_cmp_lg_u64 vcc, exec
	ds_write_b128 v200, v[52:55] offset:17408
	s_waitcnt vmcnt(4)
	ds_write2st64_b64 v202, v[64:65], v[66:67] offset0:98 offset1:106
	v_max_f32_e32 v52, 0xf149f2ca, v56
	s_cselect_b64 vcc, -1, 0
	v_cndmask_b32_e32 v150, v238, v52, vcc
	v_fma_f32 v52, v150, s4, 1.0
	v_fmamk_f32 v20, v20, 0x3e0293ee, v52
	v_exp_f32_e32 v158, v20
	v_fmamk_f32 v20, v21, 0x3e0293ee, v52
	v_exp_f32_e32 v159, v20
	v_fmamk_f32 v20, v22, 0x3e0293ee, v52
	v_exp_f32_e32 v160, v20
	v_fmamk_f32 v20, v23, 0x3e0293ee, v52
	v_exp_f32_e32 v161, v20
	v_fmamk_f32 v20, v24, 0x3e0293ee, v52
	v_exp_f32_e32 v152, v20
	v_fmamk_f32 v20, v25, 0x3e0293ee, v52
	v_exp_f32_e32 v153, v20
	v_fmamk_f32 v20, v26, 0x3e0293ee, v52
	v_exp_f32_e32 v154, v20
	v_fmamk_f32 v20, v27, 0x3e0293ee, v52
	v_exp_f32_e32 v155, v20
	v_fmamk_f32 v20, v28, 0x3e0293ee, v52
	v_exp_f32_e32 v162, v20
	v_fmamk_f32 v20, v29, 0x3e0293ee, v52
	v_exp_f32_e32 v163, v20
	v_fmamk_f32 v20, v30, 0x3e0293ee, v52
	v_exp_f32_e32 v178, v20
	v_fmamk_f32 v20, v31, 0x3e0293ee, v52
	v_exp_f32_e32 v179, v20
	v_fmamk_f32 v20, v32, 0x3e0293ee, v52
	v_exp_f32_e32 v156, v20
	v_fmamk_f32 v20, v33, 0x3e0293ee, v52
	v_pk_fma_f32 v[122:123], v[50:51], s[30:31], v[52:53] op_sel_hi:[1,0,0]
	v_pk_fma_f32 v[144:145], v[48:49], s[30:31], v[52:53] op_sel_hi:[1,0,0]
	v_pk_fma_f32 v[146:147], v[46:47], s[30:31], v[52:53] op_sel_hi:[1,0,0]
	v_pk_fma_f32 v[118:119], v[44:45], s[30:31], v[52:53] op_sel_hi:[1,0,0]
	v_pk_fma_f32 v[120:121], v[42:43], s[30:31], v[52:53] op_sel_hi:[1,0,0]
	v_pk_fma_f32 v[140:141], v[40:41], s[30:31], v[52:53] op_sel_hi:[1,0,0]
	v_pk_fma_f32 v[142:143], v[38:39], s[30:31], v[52:53] op_sel_hi:[1,0,0]
	v_pk_fma_f32 v[148:149], v[36:37], s[30:31], v[52:53] op_sel_hi:[1,0,0]
	v_exp_f32_e32 v157, v20
	v_fmamk_f32 v20, v34, 0x3e0293ee, v52
	v_fmac_f32_e32 v52, 0x3e0293ee, v35
	v_exp_f32_e32 v117, v20
	v_exp_f32_e32 v151, v52
	s_add_i32 s3, 0, 0x4400
	v_add_u32_e32 v196, s3, v70
	s_add_u32 s36, s8, s0
	v_mov_b64_e32 v[66:67], v[18:19]
	v_mov_b64_e32 v[50:51], v[18:19]
	v_mov_b64_e32 v[34:35], v[18:19]
	v_mov_b64_e32 v[82:83], v[18:19]
	s_addc_u32 s37, s9, s1
	v_mov_b64_e32 v[64:65], v[16:17]
	v_mov_b64_e32 v[62:63], v[14:15]
	v_mov_b64_e32 v[60:61], v[12:13]
	v_mov_b64_e32 v[58:59], v[10:11]
	v_mov_b64_e32 v[56:57], v[8:9]
	v_mov_b64_e32 v[54:55], v[6:7]
	v_mov_b64_e32 v[52:53], v[4:5]
	v_mov_b64_e32 v[48:49], v[16:17]
	v_mov_b64_e32 v[46:47], v[14:15]
	v_mov_b64_e32 v[44:45], v[12:13]
	v_mov_b64_e32 v[42:43], v[10:11]
	v_mov_b64_e32 v[40:41], v[8:9]
	v_mov_b64_e32 v[38:39], v[6:7]
	v_mov_b64_e32 v[36:37], v[4:5]
	v_mov_b64_e32 v[32:33], v[16:17]
	v_mov_b64_e32 v[30:31], v[14:15]
	v_mov_b64_e32 v[28:29], v[12:13]
	v_mov_b64_e32 v[26:27], v[10:11]
	v_mov_b64_e32 v[24:25], v[8:9]
	v_mov_b64_e32 v[22:23], v[6:7]
	v_mov_b64_e32 v[20:21], v[4:5]
	v_mov_b64_e32 v[80:81], v[16:17]
	v_mov_b64_e32 v[78:79], v[14:15]
	v_mov_b64_e32 v[76:77], v[12:13]
	v_mov_b64_e32 v[74:75], v[10:11]
	v_mov_b64_e32 v[72:73], v[8:9]
	v_mov_b64_e32 v[70:71], v[6:7]
	v_mov_b64_e32 v[68:69], v[4:5]
	v_mov_b32_e32 v240, v116
	v_mov_b32_e32 v241, v116
	v_mov_b32_e32 v242, v116
	v_mov_b32_e32 v243, v116
	v_mov_b32_e32 v244, v116
	v_mov_b32_e32 v245, v116
	v_mov_b32_e32 v246, v116
	v_mov_b32_e32 v247, v116
	s_waitcnt lgkmcnt(0)
	s_barrier
	s_branch .LBB0_1288

.LBB0_1288:
	ds_read_b128 v[84:87], v201 offset:50176
	ds_read_b128 v[88:91], v203 offset:50176
	ds_read_b128 v[92:95], v201 offset:54272
	ds_read_b128 v[96:99], v203 offset:54272
	ds_read_b128 v[184:187], v204 offset:50176
	ds_read_b128 v[188:191], v205 offset:50176
	ds_read_b128 v[206:209], v204 offset:54272
	ds_read_b128 v[210:213], v205 offset:54272
	v_exp_f32_e32 v118, v118
	s_waitcnt lgkmcnt(6)
	v_mfma_scale_f32_32x32x64_f8f6f4 v[100:115], v[84:91], v[124:131], 0, v226, v226 op_sel_hi:[0,0,0]
	v_exp_f32_e32 v119, v119
	v_exp_f32_e32 v146, v146
	v_exp_f32_e32 v147, v147
	v_exp_f32_e32 v148, v148
	v_exp_f32_e32 v149, v149
	v_exp_f32_e32 v182, v140
	v_exp_f32_e32 v183, v141
	v_exp_f32_e32 v180, v142
	v_exp_f32_e32 v181, v143
	v_exp_f32_e32 v120, v120
	v_exp_f32_e32 v121, v121
	s_waitcnt lgkmcnt(4)
	v_mfma_scale_f32_32x32x64_f8f6f4 v[84:99], v[92:99], v[124:131], 0, v226, v226 op_sel_hi:[0,0,0]
	v_exp_f32_e32 v122, v122
	v_exp_f32_e32 v123, v123
	v_cvt_pk_fp8_f32 v140, v158, v159
	v_cvt_pk_fp8_f32 v141, v162, v163
	v_cvt_pk_fp8_f32 v142, v152, v153
	v_cvt_pk_fp8_f32 v143, v156, v157
	v_cvt_pk_fp8_f32 v140, v160, v161 op_sel:[0,0,1]
	v_cvt_pk_fp8_f32 v141, v178, v179 op_sel:[0,0,1]
	v_cvt_pk_fp8_f32 v142, v154, v155 op_sel:[0,0,1]
	v_cvt_pk_fp8_f32 v143, v117, v151 op_sel:[0,0,1]
	v_permlane32_swap_b32_e32 v140, v141
	s_nop 0
	v_permlane32_swap_b32_e32 v142, v143
	s_waitcnt lgkmcnt(2)
	v_mfma_scale_f32_32x32x64_f8f6f4 v[100:115], v[184:191], v[132:139], v[100:115], v226, v226 op_sel_hi:[0,0,0]
	v_exp_f32_e32 v185, v145
	v_cvt_pk_fp8_f32 v145, v118, v119
	v_exp_f32_e32 v184, v144
	v_cvt_pk_fp8_f32 v144, v148, v149
	v_cvt_pk_fp8_f32 v145, v146, v147 op_sel:[0,0,1]
	v_cvt_pk_fp8_f32 v146, v182, v183
	v_cvt_pk_fp8_f32 v147, v184, v185
	v_cvt_pk_fp8_f32 v144, v180, v181 op_sel:[0,0,1]
	v_cvt_pk_fp8_f32 v146, v120, v121 op_sel:[0,0,1]
	v_cvt_pk_fp8_f32 v147, v122, v123 op_sel:[0,0,1]
	s_waitcnt lgkmcnt(0)
	v_mfma_scale_f32_32x32x64_f8f6f4 v[84:99], v[206:213], v[132:139], v[84:99], v226, v226 op_sel_hi:[0,0,0]
	v_permlane32_swap_b32_e32 v144, v145
	v_permlane32_swap_b32_e32 v146, v147
	v_lshl_add_u64 v[190:191], s[36:37], 0, v[2:3]
	s_mov_b32 s0, 0x39984000
	v_add_co_u32_e32 v118, vcc, s0, v190
	v_lshl_add_u64 v[192:193], s[36:37], 0, v[166:167]
	s_nop 0
	v_addc_co_u32_e32 v119, vcc, 0, v191, vcc
	v_add_co_u32_e32 v120, vcc, s20, v192
	v_lshl_add_u64 v[188:189], s[36:37], 0, v[168:169]
	s_nop 0
	v_addc_co_u32_e32 v121, vcc, 0, v193, vcc
	v_add_co_u32_e32 v122, vcc, s20, v188
	s_nop 1
	v_addc_co_u32_e32 v123, vcc, 0, v189, vcc
	global_load_dwordx2 v[184:185], v[118:119], off
	global_load_dwordx2 v[186:187], v[118:119], off offset:256
	global_load_dwordx2 v[178:179], v[120:121], off
	global_load_dwordx2 v[180:181], v[122:123], off
	ds_read_b64_tr_b16 v[152:153], v197 offset:0
	ds_read_b64_tr_b16 v[154:155], v197 offset:0x800
	ds_read_b64_tr_b16 v[156:157], v197 offset:0x1000
	ds_read_b64_tr_b16 v[158:159], v197 offset:0x1800
	s_waitcnt lgkmcnt(0)
	s_nop 0
	v_mfma_scale_f32_32x32x64_f8f6f4 v[4:19], v[140:147], v[152:159], v[4:19], v226, v226 op_sel_hi:[0,0,0]
	ds_read_b64_tr_b16 v[152:153], v197 offset:0x200
	ds_read_b64_tr_b16 v[154:155], v197 offset:0xa00
	ds_read_b64_tr_b16 v[156:157], v197 offset:0x1200
	ds_read_b64_tr_b16 v[158:159], v197 offset:0x1a00
	s_waitcnt lgkmcnt(0)
	s_nop 0
	v_mfma_scale_f32_32x32x64_f8f6f4 v[52:67], v[140:147], v[152:159], v[52:67], v226, v226 op_sel_hi:[0,0,0]
	ds_read_b64_tr_b16 v[152:153], v197 offset:0x400
	ds_read_b64_tr_b16 v[154:155], v197 offset:0xc00
	ds_read_b64_tr_b16 v[156:157], v197 offset:0x1400
	ds_read_b64_tr_b16 v[158:159], v197 offset:0x1c00
	s_waitcnt lgkmcnt(0)
	s_nop 0
	v_mfma_scale_f32_32x32x64_f8f6f4 v[36:51], v[140:147], v[152:159], v[36:51], v226, v226 op_sel_hi:[0,0,0]
	ds_read_b64_tr_b16 v[152:153], v197 offset:0x600
	ds_read_b64_tr_b16 v[154:155], v197 offset:0xe00
	ds_read_b64_tr_b16 v[156:157], v197 offset:0x1600
	ds_read_b64_tr_b16 v[158:159], v197 offset:0x1e00
	s_waitcnt lgkmcnt(0)
	v_mfma_scale_f32_32x32x64_f8f6f4 v[20:35], v[140:147], v[152:159], v[20:35], v226, v226 op_sel_hi:[0,0,0]
	s_barrier
	s_waitcnt vmcnt(4)
	v_mfma_scale_f32_32x32x64_f8f6f4 v[68:83], v[140:147], v[240:247], v[68:83], v226, v226 op_sel_hi:[0,0,0]
	v_max_f32_e32 v117, v100, v101
	v_max3_f32 v117, v117, v102, v103
	v_max3_f32 v117, v117, v104, v105
	v_max3_f32 v117, v117, v106, v107
	v_max3_f32 v117, v117, v108, v109
	v_max3_f32 v117, v117, v110, v111
	v_max3_f32 v117, v117, v112, v113
	v_max3_f32 v117, v117, v114, v115
	v_max3_f32 v117, v117, v84, v85
	v_max3_f32 v117, v117, v86, v87
	v_max3_f32 v117, v117, v88, v89
	v_max3_f32 v117, v117, v90, v91
	v_max3_f32 v117, v117, v92, v93
	v_max3_f32 v117, v117, v94, v95
	v_max3_f32 v117, v117, v96, v97
	v_max3_f32 v117, v117, v98, v99
	v_mov_b32_e32 v118, v117
	s_nop 1
	v_permlane32_swap_b32_e32 v117, v118
	v_max_f32_e32 v117, v117, v118
	v_sub_f32_e32 v118, v117, v150
	v_cmp_ge_f32_e32 vcc, s19, v118
	v_max_f32_e32 v117, v150, v117
	v_sub_f32_e32 v118, v150, v117
	v_mul_f32_e32 v118, 0x3e0293ee, v118
	v_exp_f32_e32 v118, v118
	s_cmp_eq_u64 vcc, exec
	s_cselect_b64 s[40:41], -1, 0
	s_waitcnt vmcnt(4)
	v_perm_b32 v120, v176, v174, s14
	v_cndmask_b32_e64 v118, v118, 1.0, s[40:41]
	v_perm_b32 v121, v176, v174, s15
	v_perm_b32 v122, v177, v175, s14
	v_perm_b32 v123, v177, v175, s15
	v_cmp_gt_f32_e32 vcc, 1.0, v118
	ds_write_b128 v200, v[120:123] offset:1024
	ds_write2st64_b64 v202, v[170:171], v[172:173] offset0:66 offset1:74
	s_cbranch_vccz .LBB0_1292
	s_and_saveexec_b64 s[0:1], s[38:39]
	ds_write_b32 v199, v118 offset:128
	s_or_b64 exec, exec, s[0:1]
	s_waitcnt lgkmcnt(0)
	v_add_u32_e32 v122, v165, v198
	ds_read_b128 v[118:121], v122 offset:224
	ds_read_b128 v[140:143], v122 offset:192
	ds_read_b128 v[144:147], v122 offset:160
	ds_read_b128 v[152:155], v122 offset:128
	s_waitcnt lgkmcnt(3)
	v_pk_mul_f32 v[16:17], v[16:17], v[118:119]
	s_waitcnt lgkmcnt(2)
	v_pk_mul_f32 v[12:13], v[12:13], v[140:141]
	s_waitcnt lgkmcnt(1)
	v_pk_mul_f32 v[8:9], v[8:9], v[144:145]
	v_pk_mul_f32 v[18:19], v[18:19], v[120:121]
	v_pk_mul_f32 v[14:15], v[14:15], v[142:143]
	v_pk_mul_f32 v[10:11], v[10:11], v[146:147]
	s_waitcnt lgkmcnt(0)
	v_pk_mul_f32 v[6:7], v[6:7], v[154:155]
	v_pk_mul_f32 v[4:5], v[4:5], v[152:153]
	v_pk_mul_f32 v[64:65], v[64:65], v[118:119]
	v_pk_mul_f32 v[60:61], v[60:61], v[140:141]
	v_pk_mul_f32 v[56:57], v[56:57], v[144:145]
	v_pk_mul_f32 v[66:67], v[66:67], v[120:121]
	v_pk_mul_f32 v[62:63], v[62:63], v[142:143]
	v_pk_mul_f32 v[58:59], v[58:59], v[146:147]
	v_pk_mul_f32 v[54:55], v[54:55], v[154:155]
	v_pk_mul_f32 v[52:53], v[52:53], v[152:153]
	v_pk_mul_f32 v[48:49], v[48:49], v[118:119]
	v_pk_mul_f32 v[44:45], v[44:45], v[140:141]
	v_pk_mul_f32 v[40:41], v[40:41], v[144:145]
	v_pk_mul_f32 v[50:51], v[50:51], v[120:121]
	v_pk_mul_f32 v[46:47], v[46:47], v[142:143]
	v_pk_mul_f32 v[42:43], v[42:43], v[146:147]
	v_pk_mul_f32 v[38:39], v[38:39], v[154:155]
	v_pk_mul_f32 v[36:37], v[36:37], v[152:153]
	v_pk_mul_f32 v[32:33], v[32:33], v[118:119]
	v_pk_mul_f32 v[28:29], v[28:29], v[140:141]
	v_pk_mul_f32 v[24:25], v[24:25], v[144:145]
	v_pk_mul_f32 v[34:35], v[34:35], v[120:121]
	v_pk_mul_f32 v[30:31], v[30:31], v[142:143]
	v_pk_mul_f32 v[26:27], v[26:27], v[146:147]
	v_pk_mul_f32 v[22:23], v[22:23], v[154:155]
	v_pk_mul_f32 v[20:21], v[20:21], v[152:153]
	v_pk_mul_f32 v[80:81], v[80:81], v[118:119]
	v_pk_mul_f32 v[76:77], v[76:77], v[140:141]
	v_pk_mul_f32 v[72:73], v[72:73], v[144:145]
	v_pk_mul_f32 v[82:83], v[82:83], v[120:121]
	v_pk_mul_f32 v[78:79], v[78:79], v[142:143]
	v_pk_mul_f32 v[74:75], v[74:75], v[146:147]
	v_pk_mul_f32 v[70:71], v[70:71], v[154:155]
	v_pk_mul_f32 v[68:69], v[68:69], v[152:153]
.LBB0_1292:
	v_cndmask_b32_e64 v206, v117, v150, s[40:41]
	v_fma_f32 v117, v206, s4, 1.0
	v_fmamk_f32 v100, v100, 0x3e0293ee, v117
	v_fmamk_f32 v101, v101, 0x3e0293ee, v117
	v_fmamk_f32 v102, v102, 0x3e0293ee, v117
	v_fmamk_f32 v145, v106, 0x3e0293ee, v117
	v_fmamk_f32 v108, v108, 0x3e0293ee, v117
	v_fmamk_f32 v109, v109, 0x3e0293ee, v117
	v_exp_f32_e32 v143, v100
	v_exp_f32_e32 v144, v101
	v_exp_f32_e32 v214, v102
	v_exp_f32_e32 v216, v145
	v_exp_f32_e32 v145, v108
	v_exp_f32_e32 v146, v109
	v_fmamk_f32 v105, v105, 0x3e0293ee, v117
	v_fmamk_f32 v110, v110, 0x3e0293ee, v117
	v_fmamk_f32 v147, v112, 0x3e0293ee, v117
	v_fmamk_f32 v103, v103, 0x3e0293ee, v117
	v_fmamk_f32 v104, v104, 0x3e0293ee, v117
	v_fmamk_f32 v107, v107, 0x3e0293ee, v117
	v_fmamk_f32 v111, v111, 0x3e0293ee, v117
	v_fmamk_f32 v148, v113, 0x3e0293ee, v117
	v_fmamk_f32 v149, v114, 0x3e0293ee, v117
	v_fmamk_f32 v150, v115, 0x3e0293ee, v117
	v_fmamk_f32 v140, v94, 0x3e0293ee, v117
	v_fmamk_f32 v141, v95, 0x3e0293ee, v117
	v_fmamk_f32 v142, v96, 0x3e0293ee, v117
	v_exp_f32_e32 v220, v105
	v_exp_f32_e32 v219, v110
	v_exp_f32_e32 v224, v147
	v_fmamk_f32 v147, v97, 0x3e0293ee, v117
	v_fmamk_f32 v112, v84, 0x3e0293ee, v117
	v_fmamk_f32 v113, v85, 0x3e0293ee, v117
	v_fmamk_f32 v114, v86, 0x3e0293ee, v117
	v_fmamk_f32 v115, v87, 0x3e0293ee, v117
	v_fmamk_f32 v118, v88, 0x3e0293ee, v117
	v_fmamk_f32 v119, v89, 0x3e0293ee, v117
	v_fmamk_f32 v120, v90, 0x3e0293ee, v117
	v_fmamk_f32 v121, v91, 0x3e0293ee, v117
	v_fmamk_f32 v122, v92, 0x3e0293ee, v117
	v_fmamk_f32 v123, v93, 0x3e0293ee, v117
	v_exp_f32_e32 v215, v103
	v_exp_f32_e32 v218, v104
	v_exp_f32_e32 v217, v107
	v_exp_f32_e32 v221, v111
	v_exp_f32_e32 v225, v148
	v_exp_f32_e32 v222, v149
	v_exp_f32_e32 v223, v150
	v_fmamk_f32 v207, v98, 0x3e0293ee, v117
	v_fmac_f32_e32 v117, 0x3e0293ee, v99
	s_waitcnt lgkmcnt(0)
	s_barrier
	ds_read_b128 v[92:95], v201 offset:33792
	ds_read_b128 v[84:87], v201 offset:37888
	ds_read_b128 v[96:99], v203 offset:33792
	ds_read_b128 v[88:91], v203 offset:37888
	ds_read_b128 v[156:159], v204 offset:33792
	ds_read_b128 v[148:151], v204 offset:37888
	ds_read_b128 v[160:163], v205 offset:33792
	ds_read_b128 v[152:155], v205 offset:37888
	v_exp_f32_e32 v230, v112
	v_exp_f32_e32 v231, v113
	v_exp_f32_e32 v232, v114
	v_exp_f32_e32 v233, v115
	v_exp_f32_e32 v118, v118
	v_exp_f32_e32 v119, v119
	s_waitcnt lgkmcnt(5)
	v_mfma_scale_f32_32x32x64_f8f6f4 v[100:115], v[92:99], v[124:131], 0, v226, v226 op_sel_hi:[0,0,0]
	v_exp_f32_e32 v122, v122
	v_exp_f32_e32 v123, v123
	v_exp_f32_e32 v208, v142
	v_exp_f32_e32 v209, v147
	v_exp_f32_e32 v182, v140
	v_exp_f32_e32 v183, v141
	v_cvt_pk_fp8_f32 v140, v143, v144
	v_cvt_pk_fp8_f32 v141, v145, v146
	v_exp_f32_e32 v120, v120
	v_exp_f32_e32 v121, v121
	s_waitcnt lgkmcnt(4)
	v_mfma_scale_f32_32x32x64_f8f6f4 v[84:99], v[84:91], v[124:131], 0, v226, v226 op_sel_hi:[0,0,0]
	v_exp_f32_e32 v207, v207
	v_exp_f32_e32 v117, v117
	v_cvt_pk_fp8_f32 v142, v218, v220
	v_cvt_pk_fp8_f32 v143, v224, v225
	v_cvt_pk_fp8_f32 v144, v230, v231
	v_cvt_pk_fp8_f32 v145, v122, v123
	v_cvt_pk_fp8_f32 v146, v118, v119
	v_cvt_pk_fp8_f32 v147, v208, v209
	v_cvt_pk_fp8_f32 v140, v214, v215 op_sel:[0,0,1]
	v_cvt_pk_fp8_f32 v141, v219, v221 op_sel:[0,0,1]
	v_cvt_pk_fp8_f32 v142, v216, v217 op_sel:[0,0,1]
	v_cvt_pk_fp8_f32 v143, v222, v223 op_sel:[0,0,1]
	s_waitcnt lgkmcnt(1)
	v_mfma_scale_f32_32x32x64_f8f6f4 v[100:115], v[156:163], v[132:139], v[100:115], v226, v226 op_sel_hi:[0,0,0]
	v_cvt_pk_fp8_f32 v144, v232, v233 op_sel:[0,0,1]
	v_cvt_pk_fp8_f32 v145, v182, v183 op_sel:[0,0,1]
	v_cvt_pk_fp8_f32 v146, v120, v121 op_sel:[0,0,1]
	v_cvt_pk_fp8_f32 v147, v207, v117 op_sel:[0,0,1]
	v_permlane32_swap_b32_e32 v140, v141
	v_permlane32_swap_b32_e32 v142, v143
	s_waitcnt lgkmcnt(0)
	v_mfma_scale_f32_32x32x64_f8f6f4 v[84:99], v[148:155], v[132:139], v[84:99], v226, v226 op_sel_hi:[0,0,0]
	v_permlane32_swap_b32_e32 v144, v145
	v_permlane32_swap_b32_e32 v146, v147
	s_add_i32 s49, s49, 2
	s_cmp_ge_u32 s49, s48
	s_cselect_b64 s[42:43], -1, 0
	s_and_b64 vcc, exec, s[42:43]
	s_cbranch_vccnz .LBB0_1294
	v_add_co_u32_e32 v230, vcc, 0x39988000, v190
	s_nop 1
	v_addc_co_u32_e32 v231, vcc, 0, v191, vcc
	v_add_co_u32_e32 v232, vcc, 0x38888000, v192
	s_nop 1
	v_addc_co_u32_e32 v233, vcc, 0, v193, vcc
	v_add_co_u32_e32 v234, vcc, 0x38888000, v188
	s_nop 1
	v_addc_co_u32_e32 v235, vcc, 0, v189, vcc
	global_load_dwordx2 v[174:175], v[230:231], off
	global_load_dwordx2 v[176:177], v[230:231], off offset:256
	global_load_dwordx2 v[170:171], v[232:233], off
	global_load_dwordx2 v[172:173], v[234:235], off
.LBB0_1294:
	ds_read_b64_tr_b16 v[148:149], v196 offset:0
	ds_read_b64_tr_b16 v[150:151], v196 offset:0x800
	ds_read_b64_tr_b16 v[152:153], v196 offset:0x1000
	ds_read_b64_tr_b16 v[154:155], v196 offset:0x1800
	s_waitcnt lgkmcnt(0)
	s_nop 0
	v_mfma_scale_f32_32x32x64_f8f6f4 v[4:19], v[140:147], v[148:155], v[4:19], v226, v226 op_sel_hi:[0,0,0]
	ds_read_b64_tr_b16 v[148:149], v196 offset:0x200
	ds_read_b64_tr_b16 v[150:151], v196 offset:0xa00
	ds_read_b64_tr_b16 v[152:153], v196 offset:0x1200
	ds_read_b64_tr_b16 v[154:155], v196 offset:0x1a00
	s_waitcnt lgkmcnt(0)
	s_nop 0
	v_mfma_scale_f32_32x32x64_f8f6f4 v[52:67], v[140:147], v[148:155], v[52:67], v226, v226 op_sel_hi:[0,0,0]
	ds_read_b64_tr_b16 v[148:149], v196 offset:0x400
	ds_read_b64_tr_b16 v[150:151], v196 offset:0xc00
	ds_read_b64_tr_b16 v[152:153], v196 offset:0x1400
	ds_read_b64_tr_b16 v[154:155], v196 offset:0x1c00
	s_waitcnt lgkmcnt(0)
	s_nop 0
	v_mfma_scale_f32_32x32x64_f8f6f4 v[36:51], v[140:147], v[148:155], v[36:51], v226, v226 op_sel_hi:[0,0,0]
	ds_read_b64_tr_b16 v[148:149], v196 offset:0x600
	ds_read_b64_tr_b16 v[150:151], v196 offset:0xe00
	ds_read_b64_tr_b16 v[152:153], v196 offset:0x1600
	ds_read_b64_tr_b16 v[154:155], v196 offset:0x1e00
	s_waitcnt lgkmcnt(0)
	v_mfma_scale_f32_32x32x64_f8f6f4 v[20:35], v[140:147], v[148:155], v[20:35], v226, v226 op_sel_hi:[0,0,0]
	s_barrier
	s_waitcnt vmcnt(4)
	v_mfma_scale_f32_32x32x64_f8f6f4 v[68:83], v[140:147], v[240:247], v[68:83], v226, v226 op_sel_hi:[0,0,0]
	s_nop 1
	v_max_f32_e32 v117, v100, v101
	v_max3_f32 v117, v117, v102, v103
	v_max3_f32 v117, v117, v104, v105
	v_max3_f32 v117, v117, v106, v107
	v_max3_f32 v117, v117, v108, v109
	v_max3_f32 v117, v117, v110, v111
	v_max3_f32 v117, v117, v112, v113
	v_max3_f32 v117, v117, v114, v115
	v_max3_f32 v117, v117, v84, v85
	v_max3_f32 v117, v117, v86, v87
	v_max3_f32 v117, v117, v88, v89
	v_max3_f32 v117, v117, v90, v91
	v_max3_f32 v117, v117, v92, v93
	v_max3_f32 v117, v117, v94, v95
	v_max3_f32 v117, v117, v96, v97
	v_max3_f32 v117, v117, v98, v99
	v_mov_b32_e32 v118, v117
	s_nop 1
	v_permlane32_swap_b32_e32 v117, v118
	v_max_f32_e32 v117, v117, v118
	v_sub_f32_e32 v118, v117, v206
	v_cmp_ge_f32_e32 vcc, s19, v118
	v_max_f32_e32 v117, v206, v117
	v_sub_f32_e32 v118, v206, v117
	v_mul_f32_e32 v118, 0x3e0293ee, v118
	v_exp_f32_e32 v118, v118
	s_cmp_eq_u64 vcc, exec
	s_cselect_b64 s[40:41], -1, 0
	s_waitcnt vmcnt(2)
	v_perm_b32 v120, v186, v184, s14
	v_cndmask_b32_e64 v118, v118, 1.0, s[40:41]
	v_perm_b32 v121, v186, v184, s15
	v_perm_b32 v122, v187, v185, s14
	v_perm_b32 v123, v187, v185, s15
	v_cmp_gt_f32_e32 vcc, 1.0, v118
	ds_write_b128 v200, v[120:123] offset:17408
	s_waitcnt vmcnt(0)
	ds_write2st64_b64 v202, v[178:179], v[180:181] offset0:98 offset1:106
	s_cbranch_vccz .LBB0_1287
	s_and_saveexec_b64 s[0:1], s[38:39]
	s_cbranch_execz .LBB0_1286
	ds_write_b32 v199, v118 offset:128
	s_branch .LBB0_1286
